# scores GEMM (P11) now uses all 256 workgroups: workgroups c and c+128 share a tile, each computes and stores one 128-row half
# speedup vs baseline: 1.0016x; 1.0016x over previous
.LBB0_891:
	s_cmp_lt_i32 s68, 12
	s_cselect_b64 s[0:1], -1, 0
	s_cmp_gt_i32 s69, 11
	s_cselect_b64 s[4:5], -1, 0
	s_and_b64 s[0:1], s[0:1], s[4:5]
	s_andn2_b64 vcc, exec, s[0:1]
	s_cbranch_vccnz .LBB0_1003
	v_mov_b32_e32 v1, v0
	s_lshr_b32 s100, s2, 7
	s_and_b32 s2, s2, 0x7f
	s_cmp_eq_u32 s100, 0
	s_cselect_b64 s[98:99], -1, 0
	s_cselect_b64 s[100:101], 0, -1
	s_cmpk_gt_i32 s2, 0x7f
	v_readfirstlane_b32 s28, v0
	s_cbranch_scc1 .LBB0_949
	s_ashr_i32 s29, s2, 31
	s_lshr_b32 s0, s29, 29
	s_add_i32 s4, s2, s0
	s_and_b32 s0, s4, -8
	s_sub_i32 s5, s2, s0
	s_cmp_gt_i32 s5, -1
	s_cbranch_scc0 .LBB0_895
	s_lshl_b32 s3, s5, 4
	s_cbranch_execz .LBB0_896
	s_branch .LBB0_897

.LBB0_907:
	v_add_u32_e32 v166, s43, v131
	v_add_u32_e32 v182, s44, v131
	s_add_u32 s22, s8, s20
	ds_read_b128 v[154:157], v166
	ds_read_b128 v[158:161], v166 offset:1024
	ds_read_b128 v[162:165], v166 offset:2048
	ds_read_b128 v[166:169], v166 offset:3072
	ds_read_b128 v[170:173], v182
	ds_read_b128 v[174:177], v182 offset:1024
	ds_read_b128 v[178:181], v182 offset:2048
	ds_read_b128 v[182:185], v182 offset:3072
	s_addc_u32 s23, s9, s21
	s_add_u32 s22, s22, 0x100
	s_addc_u32 s23, s23, 0
	s_add_u32 s51, s46, s20
	s_addc_u32 s52, s47, s21
	s_cmpk_eq_i32 s20, 0xf00
	s_cselect_b32 s25, s15, s23
	s_cselect_b32 s24, s48, s22
	s_cselect_b32 s23, s13, s52
	s_cselect_b32 s22, s49, s51
	v_lshl_add_u64 v[218:219], v[150:151], 0, s[20:21]
	s_add_i32 m0, s7, 0xc000
	ds_read_b128 v[186:189], v133
	ds_read_b128 v[190:193], v133 offset:1024
	ds_read_b128 v[194:197], v133 offset:2048
	ds_read_b128 v[198:201], v133 offset:3072
	ds_read_b128 v[202:205], v133 offset:4096
	ds_read_b128 v[206:209], v133 offset:5120
	ds_read_b128 v[210:213], v133 offset:6144
	ds_read_b128 v[214:217], v133 offset:7168
	global_load_lds_dwordx4 v[218:219], off
	v_lshl_add_u64 v[218:219], v[152:153], 0, s[20:21]
	s_add_i32 m0, s7, 0xe000
	s_nop 0
	global_load_lds_dwordx4 v[218:219], off
	s_waitcnt vmcnt(8)
	s_waitcnt lgkmcnt(0)
	s_barrier
	s_setprio 1
	s_waitcnt lgkmcnt(0)
	s_cmp_eq_u32 s98, 0
	s_cbranch_scc1 .Lp11_skip0
	v_mfma_f32_16x16x32_bf16 v[126:129], v[154:157], v[186:189], v[126:129]
	v_mfma_f32_16x16x32_bf16 v[122:125], v[162:165], v[186:189], v[122:125]
	v_mfma_f32_16x16x32_bf16 v[114:117], v[154:157], v[194:197], v[114:117]
	v_mfma_f32_16x16x32_bf16 v[106:109], v[162:165], v[194:197], v[106:109]
	v_mfma_f32_16x16x32_bf16 v[98:101], v[154:157], v[202:205], v[98:101]
	v_mfma_f32_16x16x32_bf16 v[90:93], v[162:165], v[202:205], v[90:93]
	v_mfma_f32_16x16x32_bf16 v[82:85], v[154:157], v[210:213], v[82:85]
	v_mfma_f32_16x16x32_bf16 v[74:77], v[162:165], v[210:213], v[74:77]
	v_mfma_f32_16x16x32_bf16 v[126:129], v[158:161], v[190:193], v[126:129]
	v_mfma_f32_16x16x32_bf16 v[122:125], v[166:169], v[190:193], v[122:125]
	v_mfma_f32_16x16x32_bf16 v[114:117], v[158:161], v[198:201], v[114:117]
	v_mfma_f32_16x16x32_bf16 v[106:109], v[166:169], v[198:201], v[106:109]
	v_mfma_f32_16x16x32_bf16 v[98:101], v[158:161], v[206:209], v[98:101]
	v_mfma_f32_16x16x32_bf16 v[90:93], v[166:169], v[206:209], v[90:93]
	v_mfma_f32_16x16x32_bf16 v[82:85], v[158:161], v[214:217], v[82:85]
	v_mfma_f32_16x16x32_bf16 v[74:77], v[166:169], v[214:217], v[74:77]
	s_setprio 0
	s_setprio 1
	v_mfma_f32_16x16x32_bf16 v[118:121], v[170:173], v[186:189], v[118:121]
	v_mfma_f32_16x16x32_bf16 v[110:113], v[178:181], v[186:189], v[110:113]
	v_mfma_f32_16x16x32_bf16 v[102:105], v[170:173], v[194:197], v[102:105]
	v_mfma_f32_16x16x32_bf16 v[94:97], v[178:181], v[194:197], v[94:97]
	v_mfma_f32_16x16x32_bf16 v[86:89], v[170:173], v[202:205], v[86:89]
	v_mfma_f32_16x16x32_bf16 v[78:81], v[178:181], v[202:205], v[78:81]
	v_mfma_f32_16x16x32_bf16 v[70:73], v[170:173], v[210:213], v[70:73]
	v_mfma_f32_16x16x32_bf16 v[66:69], v[178:181], v[210:213], v[66:69]
	v_mfma_f32_16x16x32_bf16 v[118:121], v[174:177], v[190:193], v[118:121]
	v_mfma_f32_16x16x32_bf16 v[110:113], v[182:185], v[190:193], v[110:113]
	v_mfma_f32_16x16x32_bf16 v[102:105], v[174:177], v[198:201], v[102:105]
	v_mfma_f32_16x16x32_bf16 v[94:97], v[182:185], v[198:201], v[94:97]
	v_mfma_f32_16x16x32_bf16 v[86:89], v[174:177], v[206:209], v[86:89]
	v_mfma_f32_16x16x32_bf16 v[78:81], v[182:185], v[206:209], v[78:81]
	v_mfma_f32_16x16x32_bf16 v[70:73], v[174:177], v[214:217], v[70:73]
	v_mfma_f32_16x16x32_bf16 v[66:69], v[182:185], v[214:217], v[66:69]
.Lp11_skip0:
	s_setprio 0
	s_barrier
	s_add_i32 s51, s43, s36
	v_lshl_add_u64 v[218:219], s[22:23], 0, v[136:137]
	s_mov_b32 m0, s51
	ds_read_b128 v[186:189], v133 offset:16384
	ds_read_b128 v[190:193], v133 offset:17408
	ds_read_b128 v[194:197], v133 offset:18432
	ds_read_b128 v[198:201], v133 offset:19456
	ds_read_b128 v[202:205], v133 offset:20480
	ds_read_b128 v[206:209], v133 offset:21504
	ds_read_b128 v[210:213], v133 offset:22528
	ds_read_b128 v[214:217], v133 offset:23552
	global_load_lds_dwordx4 v[218:219], off
	s_add_i32 m0, s51, 0x2000
	s_add_u32 s52, s22, 0x80000
	v_lshl_add_u64 v[220:221], s[22:23], 0, v[140:141]
	s_addc_u32 s53, s23, 0
	s_add_i32 s51, s44, s36
	global_load_lds_dwordx4 v[220:221], off
	v_lshl_add_u64 v[222:223], s[52:53], 0, v[136:137]
	s_mov_b32 m0, s51
	v_lshl_add_u64 v[224:225], s[24:25], 0, v[138:139]
	global_load_lds_dwordx4 v[222:223], off
	v_lshl_add_u64 v[222:223], s[52:53], 0, v[140:141]
	s_add_i32 m0, s51, 0x2000
	s_nop 0
	global_load_lds_dwordx4 v[222:223], off
	v_lshl_add_u64 v[222:223], s[24:25], 0, v[134:135]
	s_mov_b32 m0, s7
	s_nop 0
	global_load_lds_dwordx4 v[222:223], off
	s_mov_b32 m0, s37
	s_nop 0
	global_load_lds_dwordx4 v[224:225], off
	s_waitcnt vmcnt(8)
	s_waitcnt lgkmcnt(0)
	s_barrier
	s_setprio 1
	s_waitcnt lgkmcnt(0)
	s_cmp_eq_u32 s100, 0
	s_cbranch_scc1 .Lp11_skip1
	v_mfma_f32_16x16x32_bf16 v[62:65], v[154:157], v[186:189], v[62:65]
	v_mfma_f32_16x16x32_bf16 v[58:61], v[162:165], v[186:189], v[58:61]
	v_mfma_f32_16x16x32_bf16 v[50:53], v[154:157], v[194:197], v[50:53]
	v_mfma_f32_16x16x32_bf16 v[42:45], v[162:165], v[194:197], v[42:45]
	v_mfma_f32_16x16x32_bf16 v[34:37], v[154:157], v[202:205], v[34:37]
	v_mfma_f32_16x16x32_bf16 v[26:29], v[162:165], v[202:205], v[26:29]
	v_mfma_f32_16x16x32_bf16 v[18:21], v[154:157], v[210:213], v[18:21]
	v_mfma_f32_16x16x32_bf16 v[10:13], v[162:165], v[210:213], v[10:13]
	v_mfma_f32_16x16x32_bf16 v[62:65], v[158:161], v[190:193], v[62:65]
	v_mfma_f32_16x16x32_bf16 v[58:61], v[166:169], v[190:193], v[58:61]
	v_mfma_f32_16x16x32_bf16 v[50:53], v[158:161], v[198:201], v[50:53]
	v_mfma_f32_16x16x32_bf16 v[42:45], v[166:169], v[198:201], v[42:45]
	v_mfma_f32_16x16x32_bf16 v[34:37], v[158:161], v[206:209], v[34:37]
	v_mfma_f32_16x16x32_bf16 v[26:29], v[166:169], v[206:209], v[26:29]
	v_mfma_f32_16x16x32_bf16 v[18:21], v[158:161], v[214:217], v[18:21]
	v_mfma_f32_16x16x32_bf16 v[10:13], v[166:169], v[214:217], v[10:13]
	s_setprio 0
	s_setprio 1
	v_mfma_f32_16x16x32_bf16 v[54:57], v[170:173], v[186:189], v[54:57]
	v_mfma_f32_16x16x32_bf16 v[46:49], v[178:181], v[186:189], v[46:49]
	v_mfma_f32_16x16x32_bf16 v[38:41], v[170:173], v[194:197], v[38:41]
	v_mfma_f32_16x16x32_bf16 v[30:33], v[178:181], v[194:197], v[30:33]
	v_mfma_f32_16x16x32_bf16 v[22:25], v[170:173], v[202:205], v[22:25]
	v_mfma_f32_16x16x32_bf16 v[14:17], v[178:181], v[202:205], v[14:17]
	v_mfma_f32_16x16x32_bf16 v[6:9], v[170:173], v[210:213], v[6:9]
	v_mfma_f32_16x16x32_bf16 v[2:5], v[178:181], v[210:213], v[2:5]
	v_mfma_f32_16x16x32_bf16 v[54:57], v[174:177], v[190:193], v[54:57]
	v_mfma_f32_16x16x32_bf16 v[46:49], v[182:185], v[190:193], v[46:49]
	v_mfma_f32_16x16x32_bf16 v[38:41], v[174:177], v[198:201], v[38:41]
	v_mfma_f32_16x16x32_bf16 v[30:33], v[182:185], v[198:201], v[30:33]
	v_mfma_f32_16x16x32_bf16 v[22:25], v[174:177], v[206:209], v[22:25]
	v_mfma_f32_16x16x32_bf16 v[14:17], v[182:185], v[206:209], v[14:17]
	v_mfma_f32_16x16x32_bf16 v[6:9], v[174:177], v[214:217], v[6:9]
	v_mfma_f32_16x16x32_bf16 v[2:5], v[182:185], v[214:217], v[2:5]
.Lp11_skip1:
	s_setprio 0
	s_barrier
	s_add_i32 s51, 0, 0x18000
	s_add_i32 s52, 0, 0x1c000
	v_add_u32_e32 v166, s51, v131
	v_add_u32_e32 v182, s52, v131
	ds_read_b128 v[154:157], v166
	ds_read_b128 v[158:161], v166 offset:1024
	ds_read_b128 v[162:165], v166 offset:2048
	ds_read_b128 v[166:169], v166 offset:3072
	ds_read_b128 v[170:173], v182
	ds_read_b128 v[174:177], v182 offset:1024
	ds_read_b128 v[178:181], v182 offset:2048
	ds_read_b128 v[182:185], v182 offset:3072
	s_add_u32 s24, s24, 0x80000
	s_addc_u32 s25, s25, 0
	s_mov_b32 m0, s38
	v_lshl_add_u64 v[226:227], s[24:25], 0, v[134:135]
	ds_read_b128 v[186:189], v133 offset:32768
	ds_read_b128 v[190:193], v133 offset:33792
	ds_read_b128 v[194:197], v133 offset:34816
	ds_read_b128 v[198:201], v133 offset:35840
	ds_read_b128 v[202:205], v133 offset:36864
	ds_read_b128 v[206:209], v133 offset:37888
	ds_read_b128 v[210:213], v133 offset:38912
	ds_read_b128 v[214:217], v133 offset:39936
	global_load_lds_dwordx4 v[226:227], off
	v_lshl_add_u64 v[226:227], s[24:25], 0, v[138:139]
	s_mov_b32 m0, s39
	s_nop 0
	global_load_lds_dwordx4 v[226:227], off
	s_waitcnt vmcnt(8)
	s_waitcnt lgkmcnt(0)
	s_barrier
	s_setprio 1
	s_waitcnt lgkmcnt(0)
	s_cmp_eq_u32 s98, 0
	s_cbranch_scc1 .Lp11_skip2
	v_mfma_f32_16x16x32_bf16 v[126:129], v[154:157], v[186:189], v[126:129]
	v_mfma_f32_16x16x32_bf16 v[122:125], v[162:165], v[186:189], v[122:125]
	v_mfma_f32_16x16x32_bf16 v[114:117], v[154:157], v[194:197], v[114:117]
	v_mfma_f32_16x16x32_bf16 v[106:109], v[162:165], v[194:197], v[106:109]
	v_mfma_f32_16x16x32_bf16 v[98:101], v[154:157], v[202:205], v[98:101]
	v_mfma_f32_16x16x32_bf16 v[90:93], v[162:165], v[202:205], v[90:93]
	v_mfma_f32_16x16x32_bf16 v[82:85], v[154:157], v[210:213], v[82:85]
	v_mfma_f32_16x16x32_bf16 v[74:77], v[162:165], v[210:213], v[74:77]
	v_mfma_f32_16x16x32_bf16 v[126:129], v[158:161], v[190:193], v[126:129]
	v_mfma_f32_16x16x32_bf16 v[122:125], v[166:169], v[190:193], v[122:125]
	v_mfma_f32_16x16x32_bf16 v[114:117], v[158:161], v[198:201], v[114:117]
	v_mfma_f32_16x16x32_bf16 v[106:109], v[166:169], v[198:201], v[106:109]
	v_mfma_f32_16x16x32_bf16 v[98:101], v[158:161], v[206:209], v[98:101]
	v_mfma_f32_16x16x32_bf16 v[90:93], v[166:169], v[206:209], v[90:93]
	v_mfma_f32_16x16x32_bf16 v[82:85], v[158:161], v[214:217], v[82:85]
	v_mfma_f32_16x16x32_bf16 v[74:77], v[166:169], v[214:217], v[74:77]
	s_setprio 0
	s_setprio 1
	v_mfma_f32_16x16x32_bf16 v[118:121], v[170:173], v[186:189], v[118:121]
	v_mfma_f32_16x16x32_bf16 v[110:113], v[178:181], v[186:189], v[110:113]
	v_mfma_f32_16x16x32_bf16 v[102:105], v[170:173], v[194:197], v[102:105]
	v_mfma_f32_16x16x32_bf16 v[94:97], v[178:181], v[194:197], v[94:97]
	v_mfma_f32_16x16x32_bf16 v[86:89], v[170:173], v[202:205], v[86:89]
	v_mfma_f32_16x16x32_bf16 v[78:81], v[178:181], v[202:205], v[78:81]
	v_mfma_f32_16x16x32_bf16 v[70:73], v[170:173], v[210:213], v[70:73]
	v_mfma_f32_16x16x32_bf16 v[66:69], v[178:181], v[210:213], v[66:69]
	v_mfma_f32_16x16x32_bf16 v[118:121], v[174:177], v[190:193], v[118:121]
	v_mfma_f32_16x16x32_bf16 v[110:113], v[182:185], v[190:193], v[110:113]
	v_mfma_f32_16x16x32_bf16 v[102:105], v[174:177], v[198:201], v[102:105]
	v_mfma_f32_16x16x32_bf16 v[94:97], v[182:185], v[198:201], v[94:97]
	v_mfma_f32_16x16x32_bf16 v[86:89], v[174:177], v[206:209], v[86:89]
	v_mfma_f32_16x16x32_bf16 v[78:81], v[182:185], v[206:209], v[78:81]
	v_mfma_f32_16x16x32_bf16 v[70:73], v[174:177], v[214:217], v[70:73]
	v_mfma_f32_16x16x32_bf16 v[66:69], v[182:185], v[214:217], v[66:69]
.Lp11_skip2:
	s_setprio 0
	s_barrier
	s_add_i32 s24, s51, s36
	v_lshl_add_u64 v[218:219], v[218:219], 0, s[10:11]
	s_mov_b32 m0, s24
	ds_read_b128 v[186:189], v133 offset:49152
	ds_read_b128 v[190:193], v133 offset:50176
	ds_read_b128 v[194:197], v133 offset:51200
	ds_read_b128 v[198:201], v133 offset:52224
	ds_read_b128 v[202:205], v133 offset:53248
	ds_read_b128 v[206:209], v133 offset:54272
	ds_read_b128 v[210:213], v133 offset:55296
	ds_read_b128 v[214:217], v133 offset:56320
	global_load_lds_dwordx4 v[218:219], off
	s_add_i32 m0, s24, 0x2000
	s_add_u32 s22, s22, 0x80080
	v_lshl_add_u64 v[218:219], v[220:221], 0, s[10:11]
	s_addc_u32 s23, s23, 0
	s_add_i32 s24, s52, s36
	global_load_lds_dwordx4 v[218:219], off
	v_lshl_add_u64 v[218:219], s[22:23], 0, v[136:137]
	s_mov_b32 m0, s24
	s_nop 0
	global_load_lds_dwordx4 v[218:219], off
	v_lshl_add_u64 v[218:219], s[22:23], 0, v[140:141]
	s_add_i32 m0, s24, 0x2000
	s_nop 0
	global_load_lds_dwordx4 v[218:219], off
	v_lshl_add_u64 v[218:219], v[222:223], 0, s[10:11]
	s_mov_b32 m0, s40
	s_nop 0
	global_load_lds_dwordx4 v[218:219], off
	v_lshl_add_u64 v[218:219], v[224:225], 0, s[10:11]
	s_mov_b32 m0, s41
	s_nop 0
	global_load_lds_dwordx4 v[218:219], off
	s_waitcnt vmcnt(8)
	s_waitcnt lgkmcnt(0)
	s_barrier
	s_setprio 1
	s_waitcnt lgkmcnt(0)
	s_cmp_eq_u32 s100, 0
	s_cbranch_scc1 .Lp11_skip3
	v_mfma_f32_16x16x32_bf16 v[62:65], v[154:157], v[186:189], v[62:65]
	v_mfma_f32_16x16x32_bf16 v[58:61], v[162:165], v[186:189], v[58:61]
	v_mfma_f32_16x16x32_bf16 v[50:53], v[154:157], v[194:197], v[50:53]
	v_mfma_f32_16x16x32_bf16 v[42:45], v[162:165], v[194:197], v[42:45]
	v_mfma_f32_16x16x32_bf16 v[34:37], v[154:157], v[202:205], v[34:37]
	v_mfma_f32_16x16x32_bf16 v[26:29], v[162:165], v[202:205], v[26:29]
	v_mfma_f32_16x16x32_bf16 v[18:21], v[154:157], v[210:213], v[18:21]
	v_mfma_f32_16x16x32_bf16 v[10:13], v[162:165], v[210:213], v[10:13]
	v_mfma_f32_16x16x32_bf16 v[62:65], v[158:161], v[190:193], v[62:65]
	v_mfma_f32_16x16x32_bf16 v[58:61], v[166:169], v[190:193], v[58:61]
	v_mfma_f32_16x16x32_bf16 v[50:53], v[158:161], v[198:201], v[50:53]
	v_mfma_f32_16x16x32_bf16 v[42:45], v[166:169], v[198:201], v[42:45]
	v_mfma_f32_16x16x32_bf16 v[34:37], v[158:161], v[206:209], v[34:37]
	v_mfma_f32_16x16x32_bf16 v[26:29], v[166:169], v[206:209], v[26:29]
	v_mfma_f32_16x16x32_bf16 v[18:21], v[158:161], v[214:217], v[18:21]
	v_mfma_f32_16x16x32_bf16 v[10:13], v[166:169], v[214:217], v[10:13]
	s_setprio 0
	s_setprio 1
	v_mfma_f32_16x16x32_bf16 v[54:57], v[170:173], v[186:189], v[54:57]
	v_mfma_f32_16x16x32_bf16 v[46:49], v[178:181], v[186:189], v[46:49]
	v_mfma_f32_16x16x32_bf16 v[38:41], v[170:173], v[194:197], v[38:41]
	v_mfma_f32_16x16x32_bf16 v[30:33], v[178:181], v[194:197], v[30:33]
	v_mfma_f32_16x16x32_bf16 v[22:25], v[170:173], v[202:205], v[22:25]
	v_mfma_f32_16x16x32_bf16 v[14:17], v[178:181], v[202:205], v[14:17]
	v_mfma_f32_16x16x32_bf16 v[6:9], v[170:173], v[210:213], v[6:9]
	v_mfma_f32_16x16x32_bf16 v[2:5], v[178:181], v[210:213], v[2:5]
	v_mfma_f32_16x16x32_bf16 v[54:57], v[174:177], v[190:193], v[54:57]
	v_mfma_f32_16x16x32_bf16 v[46:49], v[182:185], v[190:193], v[46:49]
	v_mfma_f32_16x16x32_bf16 v[38:41], v[174:177], v[198:201], v[38:41]
	v_mfma_f32_16x16x32_bf16 v[30:33], v[182:185], v[198:201], v[30:33]
	v_mfma_f32_16x16x32_bf16 v[22:25], v[174:177], v[206:209], v[22:25]
	v_mfma_f32_16x16x32_bf16 v[14:17], v[182:185], v[206:209], v[14:17]
	v_mfma_f32_16x16x32_bf16 v[6:9], v[174:177], v[214:217], v[6:9]
	v_mfma_f32_16x16x32_bf16 v[2:5], v[182:185], v[214:217], v[2:5]
.Lp11_skip3:
	s_setprio 0
	s_barrier
	s_add_i32 s50, s50, 2
	s_add_u32 s20, s20, 0x100
	s_addc_u32 s21, s21, 0
	s_cmp_gt_u32 s50, 29
	s_cbranch_scc0 .LBB0_907
	s_add_u32 s20, s46, 0xffffff00
	s_addc_u32 s21, s47, -1
	s_andn2_b64 vcc, exec, s[4:5]
	s_cbranch_vccnz .LBB0_910
	v_mov_b32_e32 v2, 0
	s_mov_b32 s26, s12
	s_mov_b32 s6, s14
	s_mov_b64 s[8:9], s[18:19]
	s_mov_b32 s42, s45
	v_mov_b32_e32 v3, v2
	v_mov_b32_e32 v4, v2
	v_mov_b32_e32 v5, v2
	v_mov_b32_e32 v6, v2
	v_mov_b32_e32 v7, v2
	v_mov_b32_e32 v8, v2
	v_mov_b32_e32 v9, v2
	v_mov_b32_e32 v14, v2
	v_mov_b32_e32 v15, v2
	v_mov_b32_e32 v16, v2
	v_mov_b32_e32 v17, v2
	v_mov_b32_e32 v22, v2
	v_mov_b32_e32 v23, v2
	v_mov_b32_e32 v24, v2
	v_mov_b32_e32 v25, v2
	v_mov_b32_e32 v30, v2
	v_mov_b32_e32 v31, v2
	v_mov_b32_e32 v32, v2
	v_mov_b32_e32 v33, v2
	v_mov_b32_e32 v38, v2
	v_mov_b32_e32 v39, v2
	v_mov_b32_e32 v40, v2
	v_mov_b32_e32 v41, v2
	v_mov_b32_e32 v46, v2
	v_mov_b32_e32 v47, v2
	v_mov_b32_e32 v48, v2
	v_mov_b32_e32 v49, v2
	v_mov_b32_e32 v54, v2
	v_mov_b32_e32 v55, v2
	v_mov_b32_e32 v56, v2
	v_mov_b32_e32 v57, v2
	v_mov_b32_e32 v10, v2
	v_mov_b32_e32 v11, v2
	v_mov_b32_e32 v12, v2
	v_mov_b32_e32 v13, v2
	v_mov_b32_e32 v18, v2
	v_mov_b32_e32 v19, v2
	v_mov_b32_e32 v20, v2
	v_mov_b32_e32 v21, v2
	v_mov_b32_e32 v26, v2
	v_mov_b32_e32 v27, v2
	v_mov_b32_e32 v28, v2
	v_mov_b32_e32 v29, v2
	v_mov_b32_e32 v34, v2
	v_mov_b32_e32 v35, v2
	v_mov_b32_e32 v36, v2
	v_mov_b32_e32 v37, v2
	v_mov_b32_e32 v42, v2
	v_mov_b32_e32 v43, v2
	v_mov_b32_e32 v44, v2
	v_mov_b32_e32 v45, v2
	v_mov_b32_e32 v50, v2
	v_mov_b32_e32 v51, v2
	v_mov_b32_e32 v52, v2
	v_mov_b32_e32 v53, v2
	v_mov_b32_e32 v58, v2
	v_mov_b32_e32 v59, v2
	v_mov_b32_e32 v60, v2
	v_mov_b32_e32 v61, v2
	v_mov_b32_e32 v62, v2
	v_mov_b32_e32 v63, v2
	v_mov_b32_e32 v64, v2
	v_mov_b32_e32 v65, v2
	v_mov_b32_e32 v66, v2
	v_mov_b32_e32 v67, v2
	v_mov_b32_e32 v68, v2
	v_mov_b32_e32 v69, v2
	v_mov_b32_e32 v70, v2
	v_mov_b32_e32 v71, v2
	v_mov_b32_e32 v72, v2
	v_mov_b32_e32 v73, v2
	v_mov_b32_e32 v78, v2
	v_mov_b32_e32 v79, v2
	v_mov_b32_e32 v80, v2
	v_mov_b32_e32 v81, v2
	v_mov_b32_e32 v86, v2
	v_mov_b32_e32 v87, v2
	v_mov_b32_e32 v88, v2
	v_mov_b32_e32 v89, v2
	v_mov_b32_e32 v94, v2
	v_mov_b32_e32 v95, v2
	v_mov_b32_e32 v96, v2
	v_mov_b32_e32 v97, v2
	v_mov_b32_e32 v102, v2
	v_mov_b32_e32 v103, v2
	v_mov_b32_e32 v104, v2
	v_mov_b32_e32 v105, v2
	v_mov_b32_e32 v110, v2
	v_mov_b32_e32 v111, v2
	v_mov_b32_e32 v112, v2
	v_mov_b32_e32 v113, v2
	v_mov_b32_e32 v118, v2
	v_mov_b32_e32 v119, v2
	v_mov_b32_e32 v120, v2
	v_mov_b32_e32 v121, v2
	v_mov_b32_e32 v74, v2
	v_mov_b32_e32 v75, v2
	v_mov_b32_e32 v76, v2
	v_mov_b32_e32 v77, v2
	v_mov_b32_e32 v82, v2
	v_mov_b32_e32 v83, v2
	v_mov_b32_e32 v84, v2
	v_mov_b32_e32 v85, v2
	v_mov_b32_e32 v90, v2
	v_mov_b32_e32 v91, v2
	v_mov_b32_e32 v92, v2
	v_mov_b32_e32 v93, v2
	v_mov_b32_e32 v98, v2
	v_mov_b32_e32 v99, v2
	v_mov_b32_e32 v100, v2
	v_mov_b32_e32 v101, v2
	v_mov_b32_e32 v106, v2
	v_mov_b32_e32 v107, v2
	v_mov_b32_e32 v108, v2
	v_mov_b32_e32 v109, v2
	v_mov_b32_e32 v114, v2
	v_mov_b32_e32 v115, v2
	v_mov_b32_e32 v116, v2
	v_mov_b32_e32 v117, v2
	v_mov_b32_e32 v122, v2
	v_mov_b32_e32 v123, v2
	v_mov_b32_e32 v124, v2
	v_mov_b32_e32 v125, v2
	v_mov_b32_e32 v126, v2
	v_mov_b32_e32 v127, v2
	v_mov_b32_e32 v128, v2
	v_mov_b32_e32 v129, v2
	s_andn2_b64 vcc, exec, s[0:1]
	s_cbranch_vccnz .LBB0_911
	s_branch .LBB0_912

.LBB0_948:
	s_or_b64 exec, exec, s[4:5]
	s_ashr_i32 s1, s0, 31
	s_lshl_b64 s[0:1], s[0:1], 11
	s_add_u32 s4, s94, s0
	s_addc_u32 s5, s95, s1
	s_lshl_b32 s0, s26, 8
	s_ashr_i32 s1, s0, 31
	s_lshl_b64 s[0:1], s[0:1], 1
	s_add_u32 s4, s4, s0
	s_waitcnt lgkmcnt(0)
	s_barrier
	s_addc_u32 s5, s5, s1
	s_waitcnt lgkmcnt(0)
	v_mad_u64_u32 v[42:43], s[0:1], v132, 12, v[42:43]
	ds_read_b128 v[150:153], v42 offset:4096
	s_lshl_b32 s3, s3, 6
	s_add_u32 s0, s4, s3
	s_addc_u32 s1, s5, 0
	v_mov_b32_e32 v131, 0
	s_waitcnt lgkmcnt(0)
	v_mov_b32_e32 v154, v151
	v_mov_b32_e32 v155, v152
	v_mov_b32_e32 v151, v153
	v_pk_add_f32 v[150:151], v[154:155], v[150:151]
	v_lshl_add_u64 v[42:43], s[0:1], 0, v[130:131]
	v_add_f32_e32 v5, v150, v151
	v_div_scale_f32 v130, s[0:1], v5, v5, 1.0
	v_rcp_f32_e32 v133, v130
	s_mov_b64 s[0:1], 0x3c000000
	v_lshl_add_u64 v[42:43], v[42:43], 0, s[0:1]
	v_fma_f32 v150, -v130, v133, 1.0
	v_fmac_f32_e32 v133, v150, v133
	v_div_scale_f32 v150, vcc, 1.0, v5, 1.0
	v_mul_f32_e32 v151, v150, v133
	v_fma_f32 v152, -v130, v151, v150
	v_fmac_f32_e32 v151, v152, v133
	v_fma_f32 v130, -v130, v151, v150
	v_div_fmas_f32 v130, v130, v133, v151
	v_mov_b32_e32 v133, v131
	v_div_fixup_f32 v130, v130, v5, 1.0
	v_lshlrev_b64 v[132:133], 11, v[132:133]
	v_lshl_add_u64 v[132:133], v[42:43], 0, v[132:133]
	v_pk_mul_f32 v[150:151], v[8:9], v[130:131] op_sel_hi:[1,0]
	v_pk_mul_f32 v[2:3], v[2:3], v[130:131] op_sel_hi:[1,0]
	v_pk_mul_f32 v[10:11], v[10:11], v[130:131] op_sel_hi:[1,0]
	v_cvt_pk_bf16_f32 v8, v2, v3
	v_cvt_pk_bf16_f32 v9, v150, v151
	v_pk_mul_f32 v[22:23], v[22:23], v[130:131] op_sel_hi:[1,0]
	v_cvt_pk_bf16_f32 v10, v10, v11
	v_pk_mul_f32 v[6:7], v[6:7], v[130:131] op_sel_hi:[1,0]
	v_cvt_pk_bf16_f32 v11, v22, v23
	s_mov_b64 exec, s[98:99]
	global_store_dwordx4 v[132:133], v[8:11], off
	s_mov_b64 exec, -1
	v_pk_mul_f32 v[2:3], v[14:15], v[130:131] op_sel_hi:[1,0]
	v_cvt_pk_bf16_f32 v6, v6, v7
	s_nop 0
	v_pk_mul_f32 v[8:9], v[20:21], v[130:131] op_sel_hi:[1,0]
	v_pk_mul_f32 v[10:11], v[32:33], v[130:131] op_sel_hi:[1,0]
	v_cvt_pk_bf16_f32 v7, v2, v3
	v_cvt_pk_bf16_f32 v8, v8, v9
	s_nop 0
	v_cvt_pk_bf16_f32 v9, v10, v11
	ds_read_b128 v[20:23], v1 offset:4096
	s_mov_b64 exec, s[98:99]
	global_store_dwordx4 v[132:133], v[6:9], off offset:256
	s_mov_b64 exec, -1
	s_waitcnt lgkmcnt(0)
	v_mov_b32_e32 v2, v21
	v_mov_b32_e32 v3, v22
	v_mov_b32_e32 v21, v23
	v_pk_add_f32 v[2:3], v[2:3], v[20:21]
	s_nop 0
	v_add_f32_e32 v1, v2, v3
	v_div_scale_f32 v2, s[0:1], v1, v1, 1.0
	v_rcp_f32_e32 v3, v2
	s_nop 0
	v_fma_f32 v5, -v2, v3, 1.0
	v_fmac_f32_e32 v3, v5, v3
	v_div_scale_f32 v5, vcc, 1.0, v1, 1.0
	v_mul_f32_e32 v6, v5, v3
	v_fma_f32 v7, -v2, v6, v5
	v_fmac_f32_e32 v6, v7, v3
	v_fma_f32 v2, -v2, v6, v5
	v_div_fmas_f32 v2, v2, v3, v6
	v_mov_b32_e32 v5, v131
	v_div_fixup_f32 v6, v2, v1, 1.0
	v_lshlrev_b64 v[2:3], 11, v[4:5]
	v_lshl_add_u64 v[10:11], v[42:43], 0, v[2:3]
	v_pk_mul_f32 v[4:5], v[24:25], v[6:7] op_sel_hi:[1,0]
	v_pk_mul_f32 v[2:3], v[12:13], v[6:7] op_sel_hi:[1,0]
	v_pk_mul_f32 v[8:9], v[40:41], v[6:7] op_sel_hi:[1,0]
	v_pk_mul_f32 v[12:13], v[26:27], v[6:7] op_sel_hi:[1,0]
	v_cvt_pk_bf16_f32 v2, v2, v3
	v_cvt_pk_bf16_f32 v3, v4, v5
	s_nop 0
	v_cvt_pk_bf16_f32 v4, v12, v13
	v_cvt_pk_bf16_f32 v5, v8, v9
	s_mov_b64 exec, s[98:99]
	global_store_dwordx4 v[10:11], v[2:5], off
	s_mov_b64 exec, -1
	v_pk_mul_f32 v[8:9], v[52:53], v[6:7] op_sel_hi:[1,0]
	s_nop 0
	v_pk_mul_f32 v[4:5], v[30:31], v[6:7] op_sel_hi:[1,0]
	v_pk_mul_f32 v[2:3], v[18:19], v[6:7] op_sel_hi:[1,0]
	v_pk_mul_f32 v[6:7], v[38:39], v[6:7] op_sel_hi:[1,0]
	v_cvt_pk_bf16_f32 v2, v2, v3
	v_cvt_pk_bf16_f32 v3, v4, v5
	s_nop 0
	v_cvt_pk_bf16_f32 v4, v6, v7
	v_cvt_pk_bf16_f32 v5, v8, v9
	ds_read_b128 v[6:9], v17 offset:4096
	s_mov_b64 exec, s[98:99]
	global_store_dwordx4 v[10:11], v[2:5], off offset:256
	s_mov_b64 exec, -1
	v_mov_b32_e32 v17, v131
	s_waitcnt lgkmcnt(0)
	v_mov_b32_e32 v12, v7
	v_mov_b32_e32 v13, v8
	v_mov_b32_e32 v7, v9
	v_pk_add_f32 v[6:7], v[12:13], v[6:7]
	s_nop 0
	v_add_f32_e32 v1, v6, v7
	v_div_scale_f32 v6, s[0:1], v1, v1, 1.0
	v_rcp_f32_e32 v7, v6
	s_nop 0
	v_fma_f32 v2, -v6, v7, 1.0
	v_fmac_f32_e32 v7, v2, v7
	v_div_scale_f32 v2, vcc, 1.0, v1, 1.0
	v_mul_f32_e32 v3, v2, v7
	v_fma_f32 v4, -v6, v3, v2
	v_fmac_f32_e32 v3, v4, v7
	v_fma_f32 v2, -v6, v3, v2
	v_div_fmas_f32 v2, v2, v7, v3
	v_div_fixup_f32 v6, v2, v1, 1.0
	v_lshlrev_b64 v[2:3], 11, v[16:17]
	v_lshl_add_u64 v[10:11], v[42:43], 0, v[2:3]
	v_pk_mul_f32 v[4:5], v[44:45], v[6:7] op_sel_hi:[1,0]
	v_pk_mul_f32 v[2:3], v[28:29], v[6:7] op_sel_hi:[1,0]
	v_pk_mul_f32 v[8:9], v[60:61], v[6:7] op_sel_hi:[1,0]
	v_pk_mul_f32 v[12:13], v[46:47], v[6:7] op_sel_hi:[1,0]
	v_cvt_pk_bf16_f32 v2, v2, v3
	v_cvt_pk_bf16_f32 v3, v4, v5
	s_nop 0
	v_cvt_pk_bf16_f32 v4, v12, v13
	v_cvt_pk_bf16_f32 v5, v8, v9
	s_mov_b64 exec, s[98:99]
	global_store_dwordx4 v[10:11], v[2:5], off
	s_mov_b64 exec, -1
	v_pk_mul_f32 v[8:9], v[72:73], v[6:7] op_sel_hi:[1,0]
	s_nop 0
	v_pk_mul_f32 v[4:5], v[50:51], v[6:7] op_sel_hi:[1,0]
	v_pk_mul_f32 v[2:3], v[36:37], v[6:7] op_sel_hi:[1,0]
	v_pk_mul_f32 v[6:7], v[58:59], v[6:7] op_sel_hi:[1,0]
	v_cvt_pk_bf16_f32 v2, v2, v3
	v_cvt_pk_bf16_f32 v3, v4, v5
	s_nop 0
	v_cvt_pk_bf16_f32 v4, v6, v7
	v_cvt_pk_bf16_f32 v5, v8, v9
	ds_read_b128 v[6:9], v35 offset:4096
	s_mov_b64 exec, s[98:99]
	global_store_dwordx4 v[10:11], v[2:5], off offset:256
	s_mov_b64 exec, -1
	v_mov_b32_e32 v35, v131
	s_waitcnt lgkmcnt(0)
	v_mov_b32_e32 v12, v7
	v_mov_b32_e32 v13, v8
	v_mov_b32_e32 v7, v9
	v_pk_add_f32 v[6:7], v[12:13], v[6:7]
	s_nop 0
	v_add_f32_e32 v1, v6, v7
	v_div_scale_f32 v6, s[0:1], v1, v1, 1.0
	v_rcp_f32_e32 v7, v6
	s_nop 0
	v_fma_f32 v2, -v6, v7, 1.0
	v_fmac_f32_e32 v7, v2, v7
	v_div_scale_f32 v2, vcc, 1.0, v1, 1.0
	v_mul_f32_e32 v3, v2, v7
	v_fma_f32 v4, -v6, v3, v2
	v_fmac_f32_e32 v3, v4, v7
	v_fma_f32 v2, -v6, v3, v2
	v_div_fmas_f32 v2, v2, v7, v3
	v_div_fixup_f32 v6, v2, v1, 1.0
	v_lshlrev_b64 v[2:3], 11, v[34:35]
	v_lshl_add_u64 v[10:11], v[42:43], 0, v[2:3]
	v_pk_mul_f32 v[4:5], v[62:63], v[6:7] op_sel_hi:[1,0]
	v_pk_mul_f32 v[2:3], v[48:49], v[6:7] op_sel_hi:[1,0]
	v_pk_mul_f32 v[8:9], v[80:81], v[6:7] op_sel_hi:[1,0]
	v_pk_mul_f32 v[12:13], v[64:65], v[6:7] op_sel_hi:[1,0]
	v_cvt_pk_bf16_f32 v2, v2, v3
	v_cvt_pk_bf16_f32 v3, v4, v5
	s_nop 0
	v_cvt_pk_bf16_f32 v4, v12, v13
	v_cvt_pk_bf16_f32 v5, v8, v9
	s_mov_b64 exec, s[98:99]
	global_store_dwordx4 v[10:11], v[2:5], off
	s_mov_b64 exec, -1
	v_pk_mul_f32 v[8:9], v[94:95], v[6:7] op_sel_hi:[1,0]
	s_nop 0
	v_pk_mul_f32 v[4:5], v[70:71], v[6:7] op_sel_hi:[1,0]
	v_pk_mul_f32 v[2:3], v[56:57], v[6:7] op_sel_hi:[1,0]
	v_pk_mul_f32 v[6:7], v[78:79], v[6:7] op_sel_hi:[1,0]
	v_cvt_pk_bf16_f32 v2, v2, v3
	v_cvt_pk_bf16_f32 v3, v4, v5
	s_nop 0
	v_cvt_pk_bf16_f32 v4, v6, v7
	v_cvt_pk_bf16_f32 v5, v8, v9
	ds_read_b128 v[6:9], v55 offset:4096
	s_mov_b64 exec, s[98:99]
	global_store_dwordx4 v[10:11], v[2:5], off offset:256
	s_mov_b64 exec, -1
	v_mov_b32_e32 v55, v131
	s_waitcnt lgkmcnt(0)
	v_mov_b32_e32 v12, v7
	v_mov_b32_e32 v13, v8
	v_mov_b32_e32 v7, v9
	v_pk_add_f32 v[6:7], v[12:13], v[6:7]
	s_nop 0
	v_add_f32_e32 v1, v6, v7
	v_div_scale_f32 v6, s[0:1], v1, v1, 1.0
	v_rcp_f32_e32 v7, v6
	s_nop 0
	v_fma_f32 v2, -v6, v7, 1.0
	v_fmac_f32_e32 v7, v2, v7
	v_div_scale_f32 v2, vcc, 1.0, v1, 1.0
	v_mul_f32_e32 v3, v2, v7
	v_fma_f32 v4, -v6, v3, v2
	v_fmac_f32_e32 v3, v4, v7
	v_fma_f32 v2, -v6, v3, v2
	v_div_fmas_f32 v2, v2, v7, v3
	v_div_fixup_f32 v6, v2, v1, 1.0
	v_lshlrev_b64 v[2:3], 11, v[54:55]
	v_lshl_add_u64 v[10:11], v[42:43], 0, v[2:3]
	v_pk_mul_f32 v[4:5], v[84:85], v[6:7] op_sel_hi:[1,0]
	v_pk_mul_f32 v[2:3], v[68:69], v[6:7] op_sel_hi:[1,0]
	v_pk_mul_f32 v[8:9], v[102:103], v[6:7] op_sel_hi:[1,0]
	v_pk_mul_f32 v[12:13], v[86:87], v[6:7] op_sel_hi:[1,0]
	v_cvt_pk_bf16_f32 v2, v2, v3
	v_cvt_pk_bf16_f32 v3, v4, v5
	s_nop 0
	v_cvt_pk_bf16_f32 v4, v12, v13
	v_cvt_pk_bf16_f32 v5, v8, v9
	s_mov_b64 exec, s[100:101]
	global_store_dwordx4 v[10:11], v[2:5], off
	s_mov_b64 exec, -1
	v_pk_mul_f32 v[8:9], v[116:117], v[6:7] op_sel_hi:[1,0]
	s_nop 0
	v_pk_mul_f32 v[4:5], v[92:93], v[6:7] op_sel_hi:[1,0]
	v_pk_mul_f32 v[2:3], v[76:77], v[6:7] op_sel_hi:[1,0]
	v_pk_mul_f32 v[6:7], v[100:101], v[6:7] op_sel_hi:[1,0]
	v_cvt_pk_bf16_f32 v2, v2, v3
	v_cvt_pk_bf16_f32 v3, v4, v5
	s_nop 0
	v_cvt_pk_bf16_f32 v4, v6, v7
	v_cvt_pk_bf16_f32 v5, v8, v9
	ds_read_b128 v[6:9], v75 offset:4096
	s_mov_b64 exec, s[100:101]
	global_store_dwordx4 v[10:11], v[2:5], off offset:256
	s_mov_b64 exec, -1
	v_mov_b32_e32 v75, v131
	s_waitcnt lgkmcnt(0)
	v_mov_b32_e32 v12, v7
	v_mov_b32_e32 v13, v8
	v_mov_b32_e32 v7, v9
	v_pk_add_f32 v[6:7], v[12:13], v[6:7]
	s_nop 0
	v_add_f32_e32 v1, v6, v7
	v_div_scale_f32 v6, s[0:1], v1, v1, 1.0
	v_rcp_f32_e32 v7, v6
	s_nop 0
	v_fma_f32 v2, -v6, v7, 1.0
	v_fmac_f32_e32 v7, v2, v7
	v_div_scale_f32 v2, vcc, 1.0, v1, 1.0
	v_mul_f32_e32 v3, v2, v7
	v_fma_f32 v4, -v6, v3, v2
	v_fmac_f32_e32 v3, v4, v7
	v_fma_f32 v2, -v6, v3, v2
	v_div_fmas_f32 v2, v2, v7, v3
	v_div_fixup_f32 v6, v2, v1, 1.0
	v_lshlrev_b64 v[2:3], 11, v[74:75]
	v_lshl_add_u64 v[10:11], v[42:43], 0, v[2:3]
	v_pk_mul_f32 v[4:5], v[106:107], v[6:7] op_sel_hi:[1,0]
	v_pk_mul_f32 v[2:3], v[90:91], v[6:7] op_sel_hi:[1,0]
	v_pk_mul_f32 v[8:9], v[124:125], v[6:7] op_sel_hi:[1,0]
	v_pk_mul_f32 v[12:13], v[108:109], v[6:7] op_sel_hi:[1,0]
	v_cvt_pk_bf16_f32 v2, v2, v3
	v_cvt_pk_bf16_f32 v3, v4, v5
	s_nop 0
	v_cvt_pk_bf16_f32 v4, v12, v13
	v_cvt_pk_bf16_f32 v5, v8, v9
	s_mov_b64 exec, s[100:101]
	global_store_dwordx4 v[10:11], v[2:5], off
	s_mov_b64 exec, -1
	v_pk_mul_f32 v[8:9], v[142:143], v[6:7] op_sel_hi:[1,0]
	s_nop 0
	v_pk_mul_f32 v[4:5], v[114:115], v[6:7] op_sel_hi:[1,0]
	v_pk_mul_f32 v[2:3], v[98:99], v[6:7] op_sel_hi:[1,0]
	v_pk_mul_f32 v[6:7], v[122:123], v[6:7] op_sel_hi:[1,0]
	v_cvt_pk_bf16_f32 v2, v2, v3
	v_cvt_pk_bf16_f32 v3, v4, v5
	s_nop 0
	v_cvt_pk_bf16_f32 v4, v6, v7
	v_cvt_pk_bf16_f32 v5, v8, v9
	ds_read_b128 v[6:9], v97 offset:4096
	s_mov_b64 exec, s[100:101]
	global_store_dwordx4 v[10:11], v[2:5], off offset:256
	s_mov_b64 exec, -1
	v_mov_b32_e32 v97, v131
	s_waitcnt lgkmcnt(0)
	v_mov_b32_e32 v12, v7
	v_mov_b32_e32 v13, v8
	v_mov_b32_e32 v7, v9
	v_pk_add_f32 v[6:7], v[12:13], v[6:7]
	s_nop 0
	v_add_f32_e32 v1, v6, v7
	v_div_scale_f32 v6, s[0:1], v1, v1, 1.0
	v_rcp_f32_e32 v7, v6
	s_nop 0
	v_fma_f32 v2, -v6, v7, 1.0
	v_fmac_f32_e32 v7, v2, v7
	v_div_scale_f32 v2, vcc, 1.0, v1, 1.0
	v_mul_f32_e32 v3, v2, v7
	v_fma_f32 v4, -v6, v3, v2
	v_fmac_f32_e32 v3, v4, v7
	v_fma_f32 v2, -v6, v3, v2
	v_div_fmas_f32 v2, v2, v7, v3
	v_div_fixup_f32 v6, v2, v1, 1.0
	v_lshlrev_b64 v[2:3], 11, v[96:97]
	v_lshl_add_u64 v[10:11], v[42:43], 0, v[2:3]
	v_pk_mul_f32 v[4:5], v[128:129], v[6:7] op_sel_hi:[1,0]
	v_pk_mul_f32 v[2:3], v[112:113], v[6:7] op_sel_hi:[1,0]
	v_pk_mul_f32 v[8:9], v[146:147], v[6:7] op_sel_hi:[1,0]
	v_pk_mul_f32 v[12:13], v[134:135], v[6:7] op_sel_hi:[1,0]
	v_cvt_pk_bf16_f32 v2, v2, v3
	v_cvt_pk_bf16_f32 v3, v4, v5
	s_nop 0
	v_cvt_pk_bf16_f32 v4, v12, v13
	v_cvt_pk_bf16_f32 v5, v8, v9
	s_mov_b64 exec, s[100:101]
	global_store_dwordx4 v[10:11], v[2:5], off
	s_mov_b64 exec, -1
	v_pk_mul_f32 v[8:9], v[148:149], v[6:7] op_sel_hi:[1,0]
	s_nop 0
	v_pk_mul_f32 v[4:5], v[140:141], v[6:7] op_sel_hi:[1,0]
	v_pk_mul_f32 v[2:3], v[120:121], v[6:7] op_sel_hi:[1,0]
	v_pk_mul_f32 v[6:7], v[144:145], v[6:7] op_sel_hi:[1,0]
	v_cvt_pk_bf16_f32 v2, v2, v3
	v_cvt_pk_bf16_f32 v3, v4, v5
	s_nop 0
	v_cvt_pk_bf16_f32 v4, v6, v7
	v_cvt_pk_bf16_f32 v5, v8, v9
	ds_read_b128 v[6:9], v119 offset:4096
	s_mov_b64 exec, s[100:101]
	global_store_dwordx4 v[10:11], v[2:5], off offset:256
	s_mov_b64 exec, -1
	v_mov_b32_e32 v119, v131
	s_waitcnt lgkmcnt(0)
	v_mov_b32_e32 v12, v7
	v_mov_b32_e32 v13, v8
	v_mov_b32_e32 v7, v9
	v_pk_add_f32 v[6:7], v[12:13], v[6:7]
	s_nop 0
	v_add_f32_e32 v1, v6, v7
	v_div_scale_f32 v6, s[0:1], v1, v1, 1.0
	v_rcp_f32_e32 v7, v6
	s_nop 0
	v_fma_f32 v2, -v6, v7, 1.0
	v_fmac_f32_e32 v7, v2, v7
	v_div_scale_f32 v2, vcc, 1.0, v1, 1.0
	v_mul_f32_e32 v3, v2, v7
	v_fma_f32 v4, -v6, v3, v2
	v_fmac_f32_e32 v3, v4, v7
	v_fma_f32 v2, -v6, v3, v2
	v_div_fmas_f32 v2, v2, v7, v3
	v_div_fixup_f32 v6, v2, v1, 1.0
	v_lshlrev_b64 v[2:3], 11, v[118:119]
	v_lshl_add_u64 v[8:9], v[42:43], 0, v[2:3]
	v_pk_mul_f32 v[4:5], v[136:137], v[6:7] op_sel_hi:[1,0]
	v_pk_mul_f32 v[2:3], v[138:139], v[6:7] op_sel_hi:[1,0]
	v_pk_mul_f32 v[10:11], v[110:111], v[6:7] op_sel_hi:[1,0]
	v_pk_mul_f32 v[12:13], v[126:127], v[6:7] op_sel_hi:[1,0]
	v_cvt_pk_bf16_f32 v2, v2, v3
	v_cvt_pk_bf16_f32 v3, v4, v5
	s_nop 0
	v_cvt_pk_bf16_f32 v4, v12, v13
	v_cvt_pk_bf16_f32 v5, v10, v11
	s_mov_b64 exec, s[100:101]
	global_store_dwordx4 v[8:9], v[2:5], off
	s_mov_b64 exec, -1
	v_pk_mul_f32 v[10:11], v[66:67], v[6:7] op_sel_hi:[1,0]
	s_nop 0
	v_pk_mul_f32 v[4:5], v[88:89], v[6:7] op_sel_hi:[1,0]
	v_pk_mul_f32 v[2:3], v[104:105], v[6:7] op_sel_hi:[1,0]
	v_pk_mul_f32 v[6:7], v[82:83], v[6:7] op_sel_hi:[1,0]
	v_cvt_pk_bf16_f32 v2, v2, v3
	v_cvt_pk_bf16_f32 v3, v4, v5
	s_nop 0
	v_cvt_pk_bf16_f32 v4, v6, v7
	v_cvt_pk_bf16_f32 v5, v10, v11
	s_mov_b64 exec, s[100:101]
	global_store_dwordx4 v[8:9], v[2:5], off offset:256
	s_mov_b64 exec, -1
.LBB0_949:
	s_and_b32 s100, s100, 0x80
	s_or_b32 s2, s2, s100
	s_cmp_lt_i32 s69, 13
	s_cbranch_scc1 .LBB0_1003
	s_waitcnt vmcnt(0)
	s_waitcnt vmcnt(0) lgkmcnt(0)
	s_barrier
	s_and_saveexec_b64 s[0:1], s[62:63]
	s_cbranch_execz .LBB0_1002
	s_add_i32 s3, 0, 0x20160
	v_mov_b32_e32 v1, s3
	s_waitcnt vmcnt(0) expcnt(0) lgkmcnt(0)
	ds_read_b32 v3, v1
	s_add_i32 s3, 0, 0x20164
	v_mov_b32_e32 v1, s3
	ds_read_b32 v1, v1
	s_waitcnt lgkmcnt(1)
	v_cmp_ne_u32_e32 vcc, 0, v3
	s_cbranch_vccnz .LBB0_966
	v_readlane_b32 s4, v254, 1
	v_readlane_b32 s5, v254, 2
	s_load_dwordx2 s[8:9], s[4:5], 0x4
	s_add_u32 s4, s60, 0x1000
	s_addc_u32 s5, s61, 0
	s_add_u32 s6, s60, 0x1100
	s_addc_u32 s7, s61, 0
	s_waitcnt lgkmcnt(0)
	s_mul_i32 s3, s8, s33
	s_add_u32 s8, s60, 0x1200
	s_mul_i32 s3, s3, s9
	s_addc_u32 s9, s61, 0
	s_add_u32 s10, s60, 0x1300
	s_addc_u32 s11, s61, 0
	s_mov_b32 s18, 1
	v_mov_b32_e32 v17, 0
	s_branch .LBB0_954
